# v49 + codebook re-warmed in L2 right after the post-gather barrier (16 coalesced dummy loads per thread)
# baseline (speedup 1.0000x reference)
.LBB0_118:
	s_waitcnt vmcnt(0)
	v_lshrrev_b32_e32 v67, 4, v0
	v_mov_b32_e32 v66, 0x11100
	v_lshl_or_b32 v66, v67, 2, v66
	s_waitcnt lgkmcnt(0)
	s_barrier
	v_lshlrev_b32_e32 v149, 4, v0
	global_load_dwordx4 v[150:153], v149, s[22:23]
	s_add_u32 s92, s22, 0x1000
	s_addc_u32 s93, s23, 0
	global_load_dwordx4 v[150:153], v149, s[92:93]
	s_add_u32 s92, s22, 0x2000
	s_addc_u32 s93, s23, 0
	global_load_dwordx4 v[150:153], v149, s[92:93]
	s_add_u32 s92, s22, 0x3000
	s_addc_u32 s93, s23, 0
	global_load_dwordx4 v[150:153], v149, s[92:93]
	s_add_u32 s92, s22, 0x4000
	s_addc_u32 s93, s23, 0
	global_load_dwordx4 v[150:153], v149, s[92:93]
	s_add_u32 s92, s22, 0x5000
	s_addc_u32 s93, s23, 0
	global_load_dwordx4 v[150:153], v149, s[92:93]
	s_add_u32 s92, s22, 0x6000
	s_addc_u32 s93, s23, 0
	global_load_dwordx4 v[150:153], v149, s[92:93]
	s_add_u32 s92, s22, 0x7000
	s_addc_u32 s93, s23, 0
	global_load_dwordx4 v[150:153], v149, s[92:93]
	s_add_u32 s92, s22, 0x8000
	s_addc_u32 s93, s23, 0
	global_load_dwordx4 v[150:153], v149, s[92:93]
	s_add_u32 s92, s22, 0x9000
	s_addc_u32 s93, s23, 0
	global_load_dwordx4 v[150:153], v149, s[92:93]
	s_add_u32 s92, s22, 0xa000
	s_addc_u32 s93, s23, 0
	global_load_dwordx4 v[150:153], v149, s[92:93]
	s_add_u32 s92, s22, 0xb000
	s_addc_u32 s93, s23, 0
	global_load_dwordx4 v[150:153], v149, s[92:93]
	s_add_u32 s92, s22, 0xc000
	s_addc_u32 s93, s23, 0
	global_load_dwordx4 v[150:153], v149, s[92:93]
	s_add_u32 s92, s22, 0xd000
	s_addc_u32 s93, s23, 0
	global_load_dwordx4 v[150:153], v149, s[92:93]
	s_add_u32 s92, s22, 0xe000
	s_addc_u32 s93, s23, 0
	global_load_dwordx4 v[150:153], v149, s[92:93]
	s_add_u32 s92, s22, 0xf000
	s_addc_u32 s93, s23, 0
	global_load_dwordx4 v[150:153], v149, s[92:93]
	ds_read_b32 v66, v66
	v_mul_u32_u24_e32 v68, 0x102, v67
	v_lshlrev_b32_e32 v72, 3, v68
	s_waitcnt lgkmcnt(0)
	v_max_i32_e32 v66, 1, v66
	v_cvt_f32_u32_e32 v66, v66
	v_div_scale_f32 v69, s[0:1], v66, v66, 1.0
	v_rcp_f32_e32 v70, v69
	v_div_scale_f32 v68, vcc, 1.0, v66, 1.0
	v_fma_f32 v71, -v69, v70, 1.0
	v_fmac_f32_e32 v70, v71, v70
	v_mul_f32_e32 v71, v68, v70
	v_fma_f32 v73, -v69, v71, v68
	v_fmac_f32_e32 v71, v73, v70
	v_fma_f32 v68, -v69, v71, v68
	v_div_fmas_f32 v73, v68, v70, v71
	v_lshl_add_u32 v68, v138, 3, v72
	v_add_u32_e32 v76, 0x8000, v68
	ds_read2_b64 v[68:71], v76 offset1:16
	v_div_fixup_f32 v77, v73, v66, 1.0
	v_mul_i32_i24_e32 v73, 0xfffffbf8, v67
	v_lshlrev_b32_e32 v66, 2, v138
	v_add3_u32 v78, v72, v73, v66
	ds_read2_b64 v[72:75], v76 offset0:32 offset1:48
	s_waitcnt lgkmcnt(1)
	v_cvt_f32_f64_e32 v68, v[68:69]
	v_cvt_f32_f64_e32 v69, v[70:71]
	v_mul_f32_e32 v68, v77, v68
	v_mul_f32_e32 v69, v77, v69
	v_fma_f32 v79, v68, v68, 0
	ds_write2_b32 v78, v68, v69 offset1:16
	s_waitcnt lgkmcnt(1)
	v_cvt_f32_f64_e32 v68, v[72:73]
	v_fmac_f32_e32 v79, v69, v69
	v_mul_f32_e32 v72, v77, v68
	ds_read2_b64 v[68:71], v76 offset0:64 offset1:80
	v_cvt_f32_f64_e32 v73, v[74:75]
	v_fmac_f32_e32 v79, v72, v72
	v_mul_f32_e32 v73, v77, v73
	v_fmac_f32_e32 v79, v73, v73
	ds_write2_b32 v78, v72, v73 offset0:32 offset1:48
	ds_read2_b64 v[72:75], v76 offset0:96 offset1:112
	s_waitcnt lgkmcnt(2)
	v_cvt_f32_f64_e32 v68, v[68:69]
	v_cvt_f32_f64_e32 v69, v[70:71]
	v_mul_f32_e32 v68, v77, v68
	v_mul_f32_e32 v69, v77, v69
	v_fmac_f32_e32 v79, v68, v68
	ds_write2_b32 v78, v68, v69 offset0:64 offset1:80
	s_waitcnt lgkmcnt(1)
	v_cvt_f32_f64_e32 v68, v[72:73]
	v_fmac_f32_e32 v79, v69, v69
	v_mul_f32_e32 v72, v77, v68
	ds_read2_b64 v[68:71], v76 offset0:128 offset1:144
	v_cvt_f32_f64_e32 v73, v[74:75]
	v_fmac_f32_e32 v79, v72, v72
	v_mul_f32_e32 v73, v77, v73
	v_fmac_f32_e32 v79, v73, v73
	ds_write2_b32 v78, v72, v73 offset0:96 offset1:112
	ds_read2_b64 v[72:75], v76 offset0:160 offset1:176
	s_waitcnt lgkmcnt(2)
	v_cvt_f32_f64_e32 v68, v[68:69]
	v_cvt_f32_f64_e32 v69, v[70:71]
	v_mul_f32_e32 v68, v77, v68
	v_mul_f32_e32 v69, v77, v69
	v_fmac_f32_e32 v79, v68, v68
	ds_write2_b32 v78, v68, v69 offset0:128 offset1:144
	s_waitcnt lgkmcnt(1)
	v_cvt_f32_f64_e32 v68, v[72:73]
	v_fmac_f32_e32 v79, v69, v69
	v_mul_f32_e32 v72, v77, v68
	ds_read2_b64 v[68:71], v76 offset0:192 offset1:208
	v_cvt_f32_f64_e32 v73, v[74:75]
	v_fmac_f32_e32 v79, v72, v72
	v_mul_f32_e32 v73, v77, v73
	v_fmac_f32_e32 v79, v73, v73
	ds_write2_b32 v78, v72, v73 offset0:160 offset1:176
	ds_read2_b64 v[72:75], v76 offset0:224 offset1:240
	s_waitcnt lgkmcnt(2)
	v_cvt_f32_f64_e32 v68, v[68:69]
	v_cvt_f32_f64_e32 v69, v[70:71]
	v_mul_f32_e32 v68, v77, v68
	v_mul_f32_e32 v69, v77, v69
	v_fmac_f32_e32 v79, v68, v68
	ds_write2_b32 v78, v68, v69 offset0:192 offset1:208
	s_waitcnt lgkmcnt(1)
	v_cvt_f32_f64_e32 v68, v[72:73]
	v_fmac_f32_e32 v79, v69, v69
	v_mul_f32_e32 v68, v77, v68
	v_cvt_f32_f64_e32 v69, v[74:75]
	v_fmac_f32_e32 v79, v68, v68
	v_mul_f32_e32 v69, v77, v69
	v_fmac_f32_e32 v79, v69, v69
	ds_write2_b32 v78, v68, v69 offset0:224 offset1:240
	v_cmp_eq_u32_e32 vcc, 0, v138
	v_add_f32_dpp v68, v79, v79 quad_perm:[1,0,3,2] row_mask:0xf bank_mask:0xf bound_ctrl:1
	s_nop 1
	v_add_f32_dpp v68, v68, v68 quad_perm:[2,3,0,1] row_mask:0xf bank_mask:0xf bound_ctrl:1
	s_nop 1
	v_add_f32_dpp v68, v68, v68 row_half_mirror row_mask:0xf bank_mask:0xf bound_ctrl:1
	s_nop 1
	v_mov_b32_dpp v69, v68 row_mirror row_mask:0xf bank_mask:0xf bound_ctrl:1
	s_and_saveexec_b64 s[0:1], vcc
	v_mov_b32_e32 v70, 0x11200
	v_lshl_or_b32 v67, v67, 2, v70
	v_add_f32_e32 v68, v68, v69
	ds_write_b32 v67, v68
	s_or_b64 exec, exec, s[0:1]
	v_lshlrev_b32_e32 v67, 2, v140
	s_movk_i32 s0, 0x408
	v_mad_u32_u24 v67, v138, s0, v67
	s_waitcnt lgkmcnt(0)
	s_barrier
	ds_read2_b32 v[68:69], v67 offset1:4
	ds_read2_b32 v[70:71], v67 offset0:64 offset1:68
	ds_read2_b32 v[72:73], v67 offset0:192 offset1:196
	s_lshl_b32 s29, s17, 2
	s_lshl_b32 s0, s24, 2
	s_waitcnt lgkmcnt(2)
	v_mfma_f32_16x16x4_f32 a[0:3], v68, v62, 0
	s_add_i32 s0, s0, 0x10100
	s_waitcnt lgkmcnt(1)
	v_mfma_f32_16x16x4_f32 a[4:7], v70, v63, 0
	ds_read2_b32 v[62:63], v67 offset0:128 offset1:132
	s_waitcnt lgkmcnt(0)
	v_mfma_f32_16x16x4_f32 a[0:3], v62, v64, a[0:3]
	v_mfma_f32_16x16x4_f32 a[4:7], v72, v65, a[4:7]
	v_mfma_f32_16x16x4_f32 a[0:3], v69, v58, a[0:3]
	v_mfma_f32_16x16x4_f32 a[4:7], v71, v59, a[4:7]
	ds_read2_b32 v[58:59], v67 offset0:8 offset1:12
	v_mfma_f32_16x16x4_f32 a[0:3], v63, v60, a[0:3]
	ds_read2_b32 v[62:63], v67 offset0:200 offset1:204
	v_mfma_f32_16x16x4_f32 a[4:7], v73, v61, a[4:7]
	ds_read2_b32 v[60:61], v67 offset0:72 offset1:76
	s_waitcnt lgkmcnt(2)
	v_mfma_f32_16x16x4_f32 a[0:3], v58, v54, a[0:3]
	s_waitcnt lgkmcnt(0)
	v_mfma_f32_16x16x4_f32 a[4:7], v60, v55, a[4:7]
	ds_read2_b32 v[54:55], v67 offset0:136 offset1:140
	s_waitcnt lgkmcnt(0)
	v_mfma_f32_16x16x4_f32 a[0:3], v54, v56, a[0:3]
	v_mfma_f32_16x16x4_f32 a[4:7], v62, v57, a[4:7]
	v_mfma_f32_16x16x4_f32 a[0:3], v59, v50, a[0:3]
	v_mfma_f32_16x16x4_f32 a[4:7], v61, v51, a[4:7]
	ds_read2_b32 v[50:51], v67 offset0:16 offset1:20
	v_mfma_f32_16x16x4_f32 a[0:3], v55, v52, a[0:3]
	ds_read2_b32 v[54:55], v67 offset0:208 offset1:212
	v_mfma_f32_16x16x4_f32 a[4:7], v63, v53, a[4:7]
	ds_read2_b32 v[52:53], v67 offset0:80 offset1:84
	s_waitcnt lgkmcnt(2)
	v_mfma_f32_16x16x4_f32 a[0:3], v50, v46, a[0:3]
	s_waitcnt lgkmcnt(0)
	v_mfma_f32_16x16x4_f32 a[4:7], v52, v47, a[4:7]
	ds_read2_b32 v[46:47], v67 offset0:144 offset1:148
	s_waitcnt lgkmcnt(0)
	v_mfma_f32_16x16x4_f32 a[0:3], v46, v48, a[0:3]
	v_mfma_f32_16x16x4_f32 a[4:7], v54, v49, a[4:7]
	v_mfma_f32_16x16x4_f32 a[0:3], v51, v42, a[0:3]
	v_mfma_f32_16x16x4_f32 a[4:7], v53, v43, a[4:7]
	ds_read2_b32 v[42:43], v67 offset0:24 offset1:28
	v_mfma_f32_16x16x4_f32 a[0:3], v47, v44, a[0:3]
	ds_read2_b32 v[46:47], v67 offset0:216 offset1:220
	v_mfma_f32_16x16x4_f32 a[4:7], v55, v45, a[4:7]
	ds_read2_b32 v[44:45], v67 offset0:88 offset1:92
	s_waitcnt lgkmcnt(2)
	v_mfma_f32_16x16x4_f32 a[0:3], v42, v38, a[0:3]
	s_waitcnt lgkmcnt(0)
	v_mfma_f32_16x16x4_f32 a[4:7], v44, v39, a[4:7]
	ds_read2_b32 v[38:39], v67 offset0:152 offset1:156
	s_waitcnt lgkmcnt(0)
	v_mfma_f32_16x16x4_f32 a[0:3], v38, v40, a[0:3]
	v_mfma_f32_16x16x4_f32 a[4:7], v46, v41, a[4:7]
	v_mfma_f32_16x16x4_f32 a[0:3], v43, v34, a[0:3]
	v_mfma_f32_16x16x4_f32 a[4:7], v45, v35, a[4:7]
	ds_read2_b32 v[34:35], v67 offset0:32 offset1:36
	v_mfma_f32_16x16x4_f32 a[0:3], v39, v36, a[0:3]
	ds_read2_b32 v[38:39], v67 offset0:224 offset1:228
	v_mfma_f32_16x16x4_f32 a[4:7], v47, v37, a[4:7]
	ds_read2_b32 v[36:37], v67 offset0:96 offset1:100
	s_waitcnt lgkmcnt(2)
	v_mfma_f32_16x16x4_f32 a[0:3], v34, v30, a[0:3]
	s_waitcnt lgkmcnt(0)
	v_mfma_f32_16x16x4_f32 a[4:7], v36, v31, a[4:7]
	ds_read2_b32 v[30:31], v67 offset0:160 offset1:164
	s_waitcnt lgkmcnt(0)
	v_mfma_f32_16x16x4_f32 a[0:3], v30, v32, a[0:3]
	v_mfma_f32_16x16x4_f32 a[4:7], v38, v33, a[4:7]
	v_mfma_f32_16x16x4_f32 a[0:3], v35, v26, a[0:3]
	v_mfma_f32_16x16x4_f32 a[4:7], v37, v27, a[4:7]
	ds_read2_b32 v[26:27], v67 offset0:40 offset1:44
	v_mfma_f32_16x16x4_f32 a[0:3], v31, v28, a[0:3]
	ds_read2_b32 v[30:31], v67 offset0:232 offset1:236
	v_mfma_f32_16x16x4_f32 a[4:7], v39, v29, a[4:7]
	ds_read2_b32 v[28:29], v67 offset0:104 offset1:108
	s_waitcnt lgkmcnt(2)
	v_mfma_f32_16x16x4_f32 a[0:3], v26, v22, a[0:3]
	s_waitcnt lgkmcnt(0)
	v_mfma_f32_16x16x4_f32 a[4:7], v28, v23, a[4:7]
	ds_read2_b32 v[22:23], v67 offset0:168 offset1:172
	s_waitcnt lgkmcnt(0)
	v_mfma_f32_16x16x4_f32 a[0:3], v22, v24, a[0:3]
	v_mfma_f32_16x16x4_f32 a[4:7], v30, v25, a[4:7]
	v_mfma_f32_16x16x4_f32 a[0:3], v27, v18, a[0:3]
	v_mfma_f32_16x16x4_f32 a[4:7], v29, v19, a[4:7]
	ds_read2_b32 v[18:19], v67 offset0:48 offset1:52
	v_mfma_f32_16x16x4_f32 a[0:3], v23, v20, a[0:3]
	ds_read2_b32 v[22:23], v67 offset0:240 offset1:244
	v_mfma_f32_16x16x4_f32 a[4:7], v31, v21, a[4:7]
	ds_read2_b32 v[20:21], v67 offset0:112 offset1:116
	s_waitcnt lgkmcnt(2)
	v_mfma_f32_16x16x4_f32 a[0:3], v18, v14, a[0:3]
	s_waitcnt lgkmcnt(0)
	v_mfma_f32_16x16x4_f32 a[4:7], v20, v15, a[4:7]
	ds_read2_b32 v[14:15], v67 offset0:176 offset1:180
	s_waitcnt lgkmcnt(0)
	v_mfma_f32_16x16x4_f32 a[0:3], v14, v16, a[0:3]
	v_mfma_f32_16x16x4_f32 a[4:7], v22, v17, a[4:7]
	v_mfma_f32_16x16x4_f32 a[0:3], v19, v10, a[0:3]
	v_mfma_f32_16x16x4_f32 a[4:7], v21, v11, a[4:7]
	ds_read2_b32 v[10:11], v67 offset0:56 offset1:60
	v_mfma_f32_16x16x4_f32 a[0:3], v15, v12, a[0:3]
	ds_read2_b32 v[14:15], v67 offset0:248 offset1:252
	v_mfma_f32_16x16x4_f32 a[4:7], v23, v13, a[4:7]
	ds_read2_b32 v[12:13], v67 offset0:120 offset1:124
	s_waitcnt lgkmcnt(2)
	v_mfma_f32_16x16x4_f32 a[0:3], v10, v6, a[0:3]
	s_waitcnt lgkmcnt(0)
	v_mfma_f32_16x16x4_f32 a[4:7], v12, v7, a[4:7]
	ds_read2_b32 v[6:7], v67 offset0:184 offset1:188
	s_waitcnt lgkmcnt(0)
	v_mfma_f32_16x16x4_f32 a[0:3], v6, v8, a[0:3]
	v_mfma_f32_16x16x4_f32 a[4:7], v14, v9, a[4:7]
	v_mfma_f32_16x16x4_f32 a[0:3], v11, v2, a[0:3]
	v_mov_b32_e32 v2, 0x11300
	v_lshl_add_u32 v2, v134, 2, v2
	ds_read_b32 v2, v2
	v_mfma_f32_16x16x4_f32 a[4:7], v13, v3, a[4:7]
	v_lshlrev_b32_e32 v3, 10, v140
	v_add3_u32 v3, s0, v66, v3
	v_mfma_f32_16x16x4_f32 a[0:3], v7, v4, a[0:3]
	v_or_b32_e32 v7, s29, v140
	v_lshl_or_b32 v4, v7, 8, v66
	v_add_u32_e32 v4, 0x10100, v4
	v_mfma_f32_16x16x4_f32 a[4:7], v15, v5, a[4:7]
	s_nop 9
	v_accvgpr_read_b32 v5, a0
	v_accvgpr_read_b32 v6, a1
	v_accvgpr_read_b32 v8, a2
	v_accvgpr_read_b32 v9, a3
	v_accvgpr_read_b32 v70, a4
	v_accvgpr_read_b32 v71, a5
	v_accvgpr_read_b32 v72, a6
	v_accvgpr_read_b32 v73, a7
	v_add_f32_e32 v5, v5, v70
	v_add_f32_e32 v6, v6, v71
	v_add_f32_e32 v8, v8, v72
	v_add_f32_e32 v9, v9, v73
	s_waitcnt lgkmcnt(0)
	v_fma_f32 v5, -2.0, v5, v2
	v_fma_f32 v6, -2.0, v6, v2
	v_fma_f32 v8, -2.0, v8, v2
	v_fmac_f32_e32 v2, -2.0, v9
	ds_write2st64_b32 v3, v5, v6 offset1:1
	ds_write2st64_b32 v3, v8, v2 offset0:2 offset1:3
	s_waitcnt lgkmcnt(0)
	s_barrier
	ds_read2_b32 v[2:3], v4 offset1:16
	ds_read2_b32 v[4:5], v4 offset0:32 offset1:48
	v_or_b32_e32 v6, 16, v138
	v_or_b32_e32 v8, 32, v138
	v_or_b32_e32 v9, 48, v138
	s_waitcnt lgkmcnt(1)
	v_cmp_lt_f32_e32 vcc, v3, v2
	s_nop 1
	v_cndmask_b32_e32 v10, v2, v3, vcc
	v_cndmask_b32_e32 v6, v138, v6, vcc
	s_waitcnt lgkmcnt(0)
	v_cmp_lt_f32_e32 vcc, v4, v10
	s_nop 1
	v_cndmask_b32_e32 v10, v10, v4, vcc
	v_cndmask_b32_e32 v8, v6, v8, vcc
	v_cmp_lt_f32_e32 vcc, v5, v10
	s_nop 1
	v_cndmask_b32_e32 v6, v10, v5, vcc
	v_cndmask_b32_e32 v14, v8, v9, vcc
	s_nop 0
	v_mov_b32_dpp v9, v6 quad_perm:[1,0,3,2] row_mask:0xf bank_mask:0xf bound_ctrl:1
	v_mov_b32_dpp v8, v14 quad_perm:[1,0,3,2] row_mask:0xf bank_mask:0xf bound_ctrl:1
	v_cmp_gt_f32_e64 s[4:5], v6, v9
	v_cmp_ngt_f32_e32 vcc, v6, v9
	s_and_saveexec_b64 s[6:7], vcc
	v_cmp_eq_f32_e32 vcc, v6, v9
	v_cmp_lt_i32_e64 s[0:1], v8, v14
	s_and_b64 s[0:1], vcc, s[0:1]
	s_andn2_b64 s[4:5], s[4:5], exec
	s_and_b64 s[0:1], s[0:1], exec
	s_or_b64 s[4:5], s[4:5], s[0:1]
	s_or_b64 exec, exec, s[6:7]
	s_and_saveexec_b64 s[0:1], s[4:5]
	v_mov_b32_e32 v6, v9
	v_mov_b32_e32 v14, v8
	s_or_b64 exec, exec, s[0:1]
	v_mov_b32_dpp v9, v6 quad_perm:[2,3,0,1] row_mask:0xf bank_mask:0xf bound_ctrl:1
	v_mov_b32_dpp v8, v14 quad_perm:[2,3,0,1] row_mask:0xf bank_mask:0xf bound_ctrl:1
	v_cmp_gt_f32_e64 s[4:5], v6, v9
	v_cmp_ngt_f32_e32 vcc, v6, v9
	s_and_saveexec_b64 s[6:7], vcc
	v_cmp_eq_f32_e32 vcc, v6, v9
	v_cmp_lt_i32_e64 s[0:1], v8, v14
	s_and_b64 s[0:1], vcc, s[0:1]
	s_andn2_b64 s[4:5], s[4:5], exec
	s_and_b64 s[0:1], s[0:1], exec
	s_or_b64 s[4:5], s[4:5], s[0:1]
	s_or_b64 exec, exec, s[6:7]
	s_and_saveexec_b64 s[0:1], s[4:5]
	v_mov_b32_e32 v6, v9
	v_mov_b32_e32 v14, v8
	s_or_b64 exec, exec, s[0:1]
	v_mov_b32_dpp v9, v6 row_half_mirror row_mask:0xf bank_mask:0xf bound_ctrl:1
	v_mov_b32_dpp v8, v14 row_half_mirror row_mask:0xf bank_mask:0xf bound_ctrl:1
	v_cmp_gt_f32_e64 s[4:5], v6, v9
	v_cmp_ngt_f32_e32 vcc, v6, v9
	s_and_saveexec_b64 s[6:7], vcc
	v_cmp_eq_f32_e32 vcc, v6, v9
	v_cmp_lt_i32_e64 s[0:1], v8, v14
	s_and_b64 s[0:1], vcc, s[0:1]
	s_andn2_b64 s[4:5], s[4:5], exec
	s_and_b64 s[0:1], s[0:1], exec
	s_or_b64 s[4:5], s[4:5], s[0:1]
	s_or_b64 exec, exec, s[6:7]
	s_and_saveexec_b64 s[0:1], s[4:5]
	v_mov_b32_e32 v6, v9
	v_mov_b32_e32 v14, v8
	s_or_b64 exec, exec, s[0:1]
	v_mov_b32_dpp v8, v6 row_mirror row_mask:0xf bank_mask:0xf bound_ctrl:1
	v_mov_b32_dpp v9, v14 row_mirror row_mask:0xf bank_mask:0xf bound_ctrl:1
	v_cmp_gt_f32_e64 s[4:5], v6, v8
	v_cmp_ngt_f32_e32 vcc, v6, v8
	s_and_saveexec_b64 s[6:7], vcc
	v_cmp_eq_f32_e32 vcc, v6, v8
	v_cmp_lt_i32_e64 s[0:1], v9, v14
	s_and_b64 s[0:1], vcc, s[0:1]
	s_andn2_b64 s[4:5], s[4:5], exec
	s_and_b64 s[0:1], s[0:1], exec
	s_or_b64 s[4:5], s[4:5], s[0:1]
	s_or_b64 exec, exec, s[6:7]
	s_and_saveexec_b64 s[0:1], s[4:5]
	v_mov_b32_e32 v6, v8
	v_mov_b32_e32 v14, v9
	s_or_b64 exec, exec, s[0:1]
	v_mov_b32_e32 v8, 0x11300
	v_lshl_or_b32 v8, v1, 2, v8
	ds_read_b32 v8, v8
	v_mov_b32_e32 v9, 0x11200
	v_lshl_add_u32 v7, v7, 2, v9
	ds_read_b32 v9, v7
	v_mov_b32_e32 v13, 0x260
	s_waitcnt lgkmcnt(1)
	v_mov_b32_dpp v7, v8 quad_perm:[1,0,3,2] row_mask:0xf bank_mask:0xf bound_ctrl:1
	v_max_f32_e32 v8, v8, v8
	v_max_f32_e32 v7, v7, v7
	v_max_f32_e32 v7, v8, v7
	v_lshlrev_b32_e32 v18, 2, v139
	v_mov_b32_e32 v19, 0
	v_mov_b32_dpp v8, v7 quad_perm:[2,3,0,1] row_mask:0xf bank_mask:0xf bound_ctrl:1
	v_max_f32_e32 v8, v8, v8
	v_max_f32_e32 v7, v7, v8
	s_mov_b32 s25, 0
	s_mov_b32 s26, s25
	v_mov_b32_dpp v8, v7 row_half_mirror row_mask:0xf bank_mask:0xf bound_ctrl:1
	v_max_f32_e32 v8, v8, v8
	v_max_f32_e32 v7, v7, v8
	s_nop 1
	v_mov_b32_dpp v8, v7 row_mirror row_mask:0xf bank_mask:0xf bound_ctrl:1
	v_max_f32_e32 v8, v8, v8
	v_max_f32_e32 v7, v7, v8
	s_nop 0
	v_readlane_b32 s4, v7, 32
	v_readlane_b32 s5, v7, 48
	v_readlane_b32 s0, v7, 0
	v_readlane_b32 s1, v7, 16
	v_max_f32_e64 v7, s5, s5
	v_max_f32_e64 v8, s4, s4
	v_max_f32_e32 v7, v8, v7
	v_mov_b32_e32 v8, s1
	v_max3_f32 v8, s0, v8, v7
	s_mov_b32 s0, 0x3f800347
	s_mov_b32 s1, 0x3f8020c5
	s_waitcnt lgkmcnt(0)
	v_pk_mul_f32 v[8:9], v[8:9], s[0:1]
	s_mov_b32 s4, 0xf800000
	v_mul_f32_e32 v7, 0x4f800000, v9
	v_cmp_gt_f32_e32 vcc, s4, v9
	s_nop 1
	v_cndmask_b32_e32 v7, v9, v7, vcc
	v_sqrt_f32_e32 v10, v7
	s_nop 0
	v_add_u32_e32 v11, -1, v10
	v_fma_f32 v12, -v11, v10, v7
	v_cmp_ge_f32_e64 s[0:1], 0, v12
	v_add_u32_e32 v12, 1, v10
	s_nop 0
	v_cndmask_b32_e64 v11, v10, v11, s[0:1]
	v_fma_f32 v10, -v12, v10, v7
	v_cmp_lt_f32_e64 s[0:1], 0, v10
	s_nop 1
	v_cndmask_b32_e64 v10, v11, v12, s[0:1]
	v_mul_f32_e32 v11, 0x37800000, v10
	v_cndmask_b32_e32 v10, v10, v11, vcc
	v_mul_f32_e32 v11, 0x4f800000, v8
	v_cmp_gt_f32_e32 vcc, s4, v8
	v_cmp_class_f32_e64 s[0:1], v7, v13
	s_nop 0
	v_cndmask_b32_e32 v11, v8, v11, vcc
	v_sqrt_f32_e32 v12, v11
	v_cndmask_b32_e64 v7, v10, v7, s[0:1]
	v_add_u32_e32 v10, -1, v12
	v_fma_f32 v15, -v10, v12, v11
	v_cmp_ge_f32_e64 s[0:1], 0, v15
	v_add_u32_e32 v15, 1, v12
	s_nop 0
	v_cndmask_b32_e64 v10, v12, v10, s[0:1]
	v_fma_f32 v12, -v15, v12, v11
	v_cmp_lt_f32_e64 s[0:1], 0, v12
	s_nop 1
	v_cndmask_b32_e64 v10, v10, v15, s[0:1]
	v_mul_f32_e32 v12, 0x37800000, v10
	v_cndmask_b32_e32 v10, v10, v12, vcc
	v_cmp_class_f32_e32 vcc, v11, v13
	s_mov_b32 s0, 0x380637bd
	s_mov_b32 s1, 0x350637bd
	v_cndmask_b32_e32 v10, v10, v11, vcc
	v_mul_f32_e32 v7, v7, v10
	v_mul_f32_e32 v7, 0x3f800347, v7
	v_pk_mul_f32 v[8:9], v[8:9], s[0:1]
	s_nop 0
	v_fmamk_f32 v7, v7, 0x3888509c, v9
	v_add_f32_e32 v7, v8, v7
	v_add_f32_e32 v7, 0xda24260, v7
	v_add_f32_e32 v6, v6, v7
	v_cmp_le_f32_e64 s[8:9], v2, v6
	v_cmp_le_f32_e64 s[6:7], v3, v6
	v_cmp_le_f32_e64 s[4:5], v4, v6
	v_lshl_add_u64 v[2:3], s[22:23], 0, v[18:19]
	s_and_b32 s19, s8, 0xffff
	s_lshl_b32 s22, s6, 16
	v_cmp_le_f32_e64 s[0:1], v5, v6
	s_or_b32 s24, s19, s22
	s_and_b32 s23, s4, 0xffff
	s_mov_b32 s22, s25
	s_or_b64 s[22:23], s[24:25], s[22:23]
	s_lshl_b32 s27, s0, 16
	s_or_b64 s[26:27], s[22:23], s[26:27]
	s_add_u32 s22, s26, -1
	s_addc_u32 s23, s27, -1
	s_and_b64 s[22:23], s[26:27], s[22:23]
	s_cmp_eq_u64 s[22:23], 0
	v_readlane_b32 s22, v14, 0
	s_cbranch_scc1 .LBB0_139
	s_lshl_b32 s19, s29, 2
	s_add_i32 s19, s19, 0x11100
	v_mov_b32_e32 v4, s19
	ds_read_b32 v4, v4
	s_mul_i32 s19, s17, 0x2040
	v_add_u32_e32 v8, s19, v135
	v_mov_b32_e32 v15, 0x7f800000
	s_waitcnt lgkmcnt(0)
	v_max_i32_e32 v4, 1, v4
	v_cvt_f64_u32_e32 v[12:13], v4
	v_div_scale_f64 v[16:17], s[30:31], v[12:13], v[12:13], 1.0
	v_rcp_f64_e32 v[20:21], v[16:17]
	v_div_scale_f64 v[22:23], vcc, 1.0, v[12:13], 1.0
	ds_read2st64_b64 v[4:7], v8 offset0:64 offset1:65
	ds_read2st64_b64 v[8:11], v8 offset0:66 offset1:67
	v_fma_f64 v[24:25], -v[16:17], v[20:21], 1.0
	v_fmac_f64_e32 v[20:21], v[20:21], v[24:25]
	v_fma_f64 v[24:25], -v[16:17], v[20:21], 1.0
	v_fmac_f64_e32 v[20:21], v[20:21], v[24:25]
	v_mul_f64 v[24:25], v[22:23], v[20:21]
	v_fma_f64 v[16:17], -v[16:17], v[24:25], v[22:23]
	v_div_fmas_f64 v[16:17], v[16:17], v[20:21], v[24:25]
	v_div_fixup_f64 v[12:13], v[16:17], v[12:13], 1.0
	s_waitcnt lgkmcnt(1)
	v_mul_f64 v[6:7], v[6:7], v[12:13]
	v_mul_f64 v[4:5], v[4:5], v[12:13]
	s_waitcnt lgkmcnt(0)
	v_mul_f64 v[8:9], v[8:9], v[12:13]
	v_mul_f64 v[10:11], v[12:13], v[10:11]
	v_mul_f64 v[12:13], v[6:7], v[6:7]
	v_fmac_f64_e32 v[12:13], v[4:5], v[4:5]
	v_fmac_f64_e32 v[12:13], v[8:9], v[8:9]
	v_fmac_f64_e32 v[12:13], v[10:11], v[10:11]
	s_nop 1
	v_mov_b32_dpp v16, v12 quad_perm:[1,0,3,2] row_mask:0xf bank_mask:0xf bound_ctrl:1
	v_mov_b32_dpp v17, v13 quad_perm:[1,0,3,2] row_mask:0xf bank_mask:0xf bound_ctrl:1
	v_add_f64 v[12:13], v[12:13], v[16:17]
	s_nop 1
	v_mov_b32_dpp v16, v12 quad_perm:[2,3,0,1] row_mask:0xf bank_mask:0xf bound_ctrl:1
	v_mov_b32_dpp v17, v13 quad_perm:[2,3,0,1] row_mask:0xf bank_mask:0xf bound_ctrl:1
	v_add_f64 v[12:13], v[12:13], v[16:17]
	s_nop 1
	v_mov_b32_dpp v16, v12 row_half_mirror row_mask:0xf bank_mask:0xf bound_ctrl:1
	v_mov_b32_dpp v17, v13 row_half_mirror row_mask:0xf bank_mask:0xf bound_ctrl:1
	v_add_f64 v[12:13], v[12:13], v[16:17]
	s_nop 1
	v_mov_b32_dpp v16, v12 row_mirror row_mask:0xf bank_mask:0xf bound_ctrl:1
	v_mov_b32_dpp v17, v13 row_mirror row_mask:0xf bank_mask:0xf bound_ctrl:1
	v_add_f64 v[12:13], v[12:13], v[16:17]
	s_nop 0
	v_readlane_b32 s19, v13, 16
	v_readlane_b32 s23, v12, 16
	v_readlane_b32 s31, v13, 0
	v_readlane_b32 s30, v12, 0
	v_mov_b32_e32 v16, s23
	v_mov_b32_e32 v17, s19
	v_readlane_b32 s19, v13, 48
	v_readlane_b32 s23, v12, 48
	v_add_f64 v[16:17], s[30:31], v[16:17]
	v_readlane_b32 s31, v13, 32
	v_readlane_b32 s30, v12, 32
	v_mov_b32_e32 v12, s23
	v_mov_b32_e32 v13, s19
	v_add_f64 v[12:13], s[30:31], v[12:13]
	v_add_f64 v[12:13], v[16:17], v[12:13]
